# baseline (speedup 1.0000x reference)
_Z12graph_kerneliPKfS0_S0_PKtiS2_S2_iPti:
	s_load_dword s3, s[0:1], 0x0
	s_load_dwordx4 s[4:7], s[0:1], 0x8
	s_load_dwordx2 s[8:9], s[0:1], 0x18
	s_load_dword s15, s[0:1], 0x28
	s_load_dwordx2 s[16:17], s[0:1], 0x20
	v_readfirstlane_b32 s10, v0
	s_lshl_b32 s11, s2, 10
	s_lshr_b32 s14, s10, 6
	s_ashr_i32 s10, s2, 3
	s_and_b32 s11, s11, 0x1800
	s_bitcmp1_b32 s2, 0
	s_waitcnt lgkmcnt(0)
	s_cselect_b32 s2, s3, 0
	s_add_i32 s2, s2, s10
	s_lshl_b32 s2, s2, 2
	s_add_i32 s2, s2, s11
	s_add_i32 s12, s2, s14
	v_and_b32_e32 v74, 63, v0
	v_cmp_gt_u32_e64 s[2:3], 48, v74
	s_ashr_i32 s13, s12, 31
	v_mov_b32_e32 v0, 0
	v_lshlrev_b32_e32 v68, 4, v74
	v_mov_b32_e32 v1, 0
	v_mov_b32_e32 v2, 0
	v_mov_b32_e32 v3, 0
	s_and_saveexec_b64 s[10:11], s[2:3]
	s_cbranch_execz .LBB0_2
	s_mul_hi_i32 s19, s12, s15
	s_mul_i32 s18, s12, s15
	s_lshl_b64 s[18:19], s[18:19], 1
	s_add_u32 s16, s16, s18
	s_addc_u32 s17, s17, s19
	global_load_dwordx4 v[0:3], v68, s[16:17]

_Z13gemm8p_kernel5GArgs:
	s_load_dwordx4 s[20:23], s[0:1], 0x80
	s_load_dwordx8 s[4:11], s[0:1], 0x0
	s_load_dwordx8 s[12:19], s[0:1], 0x48
	s_load_dwordx2 s[24:25], s[0:1], 0x38
	v_and_b32_e32 v2, 32, v0
	s_waitcnt lgkmcnt(0)
	s_cmp_lt_i32 s2, s22
	s_cselect_b64 s[26:27], -1, 0
	s_and_b64 s[28:29], s[26:27], exec
	s_cselect_b32 s12, s4, s12
	s_cselect_b32 s3, s25, s21
	s_cselect_b32 s4, 0, s22
	s_cselect_b32 s13, s5, s13
	s_cselect_b32 s7, s7, s15
	s_cselect_b32 s14, s6, s14
	s_sub_i32 s2, s2, s4
	s_and_b32 s4, s2, 7
	s_lshl_b32 s5, s3, 2
	s_mul_i32 s4, s4, s5
	s_lshr_b32 s5, s2, 3
	s_add_i32 s2, s4, s5
	s_lshl_b32 s5, s3, 4
	s_cmp_ge_u32 s2, s5
	s_cselect_b32 s6, s5, 0
	s_cselect_b32 s5, 16, 0
	s_sub_i32 s2, s2, s6
	s_lshr_b32 s4, s2, 4
	s_and_b32 s2, s2, 15
	s_add_i32 s15, s2, s5
	v_bfe_u32 v155, v0, 2, 4
	v_mov_b32_e32 v3, 0
	v_lshrrev_b32_e32 v6, 3, v0
	s_branch .Lgemm_idx_pad_end
	s_nop 0
	s_nop 0
	s_nop 0
	s_nop 0
	s_nop 0
	s_nop 0
	s_nop 0
	s_nop 0
	s_nop 0
	s_nop 0
	s_nop 0
	s_nop 0
	s_nop 0
	s_nop 0
	s_nop 0
	s_nop 0
	s_nop 0
	s_nop 0
	s_nop 0
	s_nop 0
	s_nop 0
	s_nop 0
	s_nop 0
	s_nop 0
	s_nop 0
	s_nop 0
	s_nop 0
	s_nop 0
	s_nop 0
	s_nop 0
	s_nop 0
	s_nop 0
	s_nop 0
	s_nop 0
	s_nop 0
	s_nop 0
	s_nop 0
	s_nop 0
	s_nop 0
	s_nop 0
	s_nop 0
	s_nop 0
	s_nop 0
	s_nop 0
	s_nop 0
	s_nop 0
	s_nop 0
	s_nop 0
	s_nop 0
	s_nop 0
	s_nop 0
	s_nop 0
	s_nop 0
	s_nop 0
	s_nop 0
	s_nop 0
	s_nop 0
	s_nop 0
	s_nop 0
	s_nop 0
.Lgemm_idx_pad_end:
	s_lshl_b32 s2, s4, 8
	s_lshl_b32 s6, s15, 8
	s_ashr_i32 s3, s2, 31
	v_lshlrev_b32_e32 v1, 4, v0
	s_mul_i32 s4, s4, 0x30000
	v_bitop3_b32 v2, v1, v2, 48 bitop3:0x6c
	s_mul_hi_i32 s5, s2, 0x300
	s_add_u32 s4, s14, s4
	v_and_or_b32 v2, v0, 64, v2
	s_addc_u32 s5, s7, s5
	v_or_b32_e32 v38, 0x10000, v1
	v_lshl_add_u64 v[4:5], s[4:5], 0, v[2:3]
	v_and_or_b32 v7, v6, 48, v155
	v_readfirstlane_b32 s4, v38
	v_mul_u32_u24_e32 v18, 0x300, v7
	v_mov_b32_e32 v19, v3
	s_mov_b32 m0, s4
	v_or_b32_e32 v6, 64, v6
	s_movk_i32 s4, 0x70
	v_or_b32_e32 v41, 0x12000, v1
	v_lshl_add_u64 v[14:15], v[4:5], 0, v[18:19]
	v_and_or_b32 v6, v6, s4, v155
	v_readfirstlane_b32 s4, v41
	s_mul_i32 s15, s15, 0x30000
	global_load_lds_dwordx4 v[14:15], off
	s_mov_b32 m0, s4
	s_mul_hi_i32 s5, s6, 0x300
	s_add_u32 s4, s12, s15
	v_mul_u32_u24_e32 v20, 0x300, v6
	v_mov_b32_e32 v21, v3
	s_addc_u32 s5, s13, s5
	v_lshl_add_u64 v[16:17], v[4:5], 0, v[20:21]
	v_lshl_add_u64 v[4:5], s[4:5], 0, v[2:3]
	v_readfirstlane_b32 s4, v1
	v_or_b32_e32 v37, 0x2000, v1
	global_load_lds_dwordx4 v[16:17], off
	v_lshl_add_u64 v[10:11], v[4:5], 0, v[18:19]
	s_mov_b32 m0, s4
	v_readfirstlane_b32 s4, v37
	global_load_lds_dwordx4 v[10:11], off
	s_mov_b32 m0, s4
	s_or_b32 s4, s2, 0x80
	s_mul_hi_i32 s5, s4, 0x300
	s_mulk_i32 s4, 0x300
	s_add_u32 s4, s14, s4
	s_addc_u32 s5, s7, s5
	v_or_b32_e32 v35, 0x14000, v1
	v_lshl_add_u64 v[12:13], v[4:5], 0, v[20:21]
	v_lshl_add_u64 v[4:5], s[4:5], 0, v[2:3]
	v_readfirstlane_b32 s4, v35
	v_or_b32_e32 v36, 0x16000, v1
	global_load_lds_dwordx4 v[12:13], off
	v_lshl_add_u64 v[6:7], v[4:5], 0, v[18:19]
	s_mov_b32 m0, s4
	v_readfirstlane_b32 s4, v36
	global_load_lds_dwordx4 v[6:7], off
	s_mov_b32 m0, s4
	s_or_b32 s4, s6, 0x80
	s_mul_hi_i32 s5, s4, 0x300
	s_mulk_i32 s4, 0x300
	s_add_u32 s4, s12, s4
	s_addc_u32 s5, s13, s5
	v_or_b32_e32 v39, 0x4000, v1
	v_lshl_add_u64 v[8:9], v[4:5], 0, v[20:21]
	v_lshl_add_u64 v[4:5], s[4:5], 0, v[2:3]
	v_readfirstlane_b32 s4, v39
	v_or_b32_e32 v40, 0x6000, v1
	global_load_lds_dwordx4 v[8:9], off
	v_lshl_add_u64 v[2:3], v[4:5], 0, v[18:19]
	s_mov_b32 m0, s4
	v_readfirstlane_b32 s4, v40
	global_load_lds_dwordx4 v[2:3], off
	v_lshl_add_u64 v[4:5], v[4:5], 0, v[20:21]
	s_mov_b32 m0, s4
	v_lshrrev_b32_e32 v18, 8, v0
	global_load_lds_dwordx4 v[4:5], off
	v_cmp_eq_u32_e32 vcc, 1, v18
	s_and_saveexec_b64 s[4:5], vcc
	s_cbranch_execz .LBB2_2
	s_barrier
